# P6: router bias load hoisted out of the chunk loop, so the mid-chunk wait no longer drains the next chunk's prefetched row loads (vmcnt(0) -> lgkm only); on top of v60
# baseline (speedup 1.0000x reference)
.LBB0_969:
	s_andn2_b64 vcc, exec, s[6:7]
	s_mov_b32 s25, 0
	s_cbranch_vccnz .LBB0_1064
	v_mbcnt_lo_u32_b32 v128, -1, 0
	v_mbcnt_hi_u32_b32 v128, -1, v128
	v_and_b32_e32 v129, 64, v128
	v_add_u32_e32 v129, 64, v129
	v_xor_b32_e32 v131, 1, v128
	v_cmp_lt_i32_e32 vcc, v131, v129
	s_lshl_b32 s24, s58, 1
	s_lshl_b32 s3, s58, 14
	v_cndmask_b32_e32 v131, v128, v131, vcc
	v_lshlrev_b32_e32 v184, 2, v131
	v_xor_b32_e32 v131, 2, v128
	v_cmp_lt_i32_e32 vcc, v131, v129
	s_add_i32 s28, s3, 0
	s_or_b32 s3, s24, 1
	v_cndmask_b32_e32 v131, v128, v131, vcc
	v_lshlrev_b32_e32 v185, 2, v131
	v_xor_b32_e32 v131, 4, v128
	v_cmp_lt_i32_e32 vcc, v131, v129
	s_lshl_b32 s3, s3, 13
	s_add_i32 s29, s3, 0
	v_cndmask_b32_e32 v131, v128, v131, vcc
	s_lshl_b64 s[6:7], s[24:25], 12
	v_lshlrev_b32_e32 v186, 2, v131
	v_xor_b32_e32 v131, 8, v128
	s_add_u32 s1, s1, s6
	v_cmp_lt_i32_e32 vcc, v131, v129
	s_addc_u32 s2, s2, s7
	s_add_i32 s6, 0, 0x20000
	s_lshl_b32 s7, s58, 11
	v_cndmask_b32_e32 v131, v128, v131, vcc
	s_lshl_b32 s3, s58, 10
	s_add_i32 s7, s7, s6
	v_lshlrev_b32_e32 v187, 2, v131
	v_xor_b32_e32 v131, 16, v128
	s_add_u32 s16, s78, 0x10000
	v_cmp_lt_i32_e32 vcc, v131, v129
	s_addc_u32 s17, s79, 0
	s_add_u32 s18, s78, 0x200000
	v_cndmask_b32_e32 v131, v128, v131, vcc
	v_lshlrev_b32_e32 v188, 2, v131
	v_xor_b32_e32 v131, 32, v128
	s_addc_u32 s19, s79, 0
	s_load_dwordx2 s[4:5], s[4:5], 0x68
	v_cmp_lt_i32_e32 vcc, v131, v129
	s_add_u32 s20, s78, 0x600000
	s_addc_u32 s21, s79, 0
	v_cndmask_b32_e32 v128, v128, v131, vcc
	v_lshlrev_b32_e32 v189, 2, v128
	v_xor_b32_e32 v128, s24, v164
	s_add_u32 s22, s78, 0x120000
	v_mov_b32_e32 v131, 0
	v_lshlrev_b32_e32 v168, 4, v128
	v_bitop3_b32 v128, v164, s24, 1 bitop3:0x1e
	v_and_b32_e32 v190, 31, v164
	s_addc_u32 s23, s79, 0
	s_ashr_i32 s97, s96, 31
	s_lshl_b64 s[14:15], s[60:61], 6
	v_lshlrev_b32_e32 v169, 4, v128
	v_lshlrev_b32_e32 v128, 2, v190
	v_mov_b32_e32 v129, v131
	s_add_i32 s24, 0, 0x24000
	s_lshl_b32 s33, s74, 6
	s_lshl_b64 s[12:13], s[96:97], 15
	s_and_b32 s15, s15, 63
	s_and_b32 s14, s14, 0xfffff000
	v_lshl_add_u32 v171, v165, 2, s7
	s_waitcnt lgkmcnt(0)
	v_lshl_add_u64 v[164:165], s[4:5], 0, v[128:129]
	global_load_dword v246, v[164:165], off
	v_and_b32_e32 v129, 0x3fffffe0, v166
	s_add_u32 s14, s78, s14
	v_lshlrev_b32_e32 v129, 2, v129
	s_addc_u32 s15, s79, s15
	v_add3_u32 v191, s6, v129, v128
	v_ashrrev_i32_e32 v128, 3, v166
	s_add_u32 s12, s14, s12
	v_lshrrev_b32_e32 v130, 2, v130
	v_and_b32_e32 v128, -4, v128
	s_addc_u32 s13, s15, s13
	v_lshlrev_b32_e32 v170, 9, v167
	v_add_u32_e32 v128, v128, v190
	v_lshl_add_u64 v[166:167], s[12:13], 0, v[130:131]
	s_mov_b64 s[12:13], 0x40000800
	s_ashr_i32 s75, s74, 31
	v_cmp_gt_u32_e64 s[4:5], 4, v190
	v_cmp_eq_u32_e64 s[6:7], 0, v190
	v_cmp_eq_u32_e64 s[8:9], 1, v190
	v_cmp_eq_u32_e64 s[10:11], 2, v190
	v_lshl_add_u32 v192, v128, 4, s24
	v_lshl_add_u32 v128, s96, 6, v128
	v_lshl_add_u64 v[166:167], v[166:167], 0, s[12:13]
	s_lshl_b64 s[26:27], s[74:75], 15
	v_mov_b32_e32 v193, 0x358637bd
	s_mov_b32 s40, 0xf800000
	v_mov_b32_e32 v194, 0x260
	v_add_u32_e32 v195, s28, v168
	v_add_u32_e32 v196, s29, v169
	s_mov_b64 s[28:29], 0x1000
	s_movk_i32 s41, 0x1000
	s_mov_b32 s42, 0xffffffe
	v_add_u32_e32 v197, v171, v170
	v_mov_b32_e32 v198, 1
	v_mov_b32_e32 v199, 0xff800000
	s_mov_b32 s30, s96
	s_branch .LBB0_973

.LBB0_975:
	v_mbcnt_lo_u32_b32 v129, -1, 0
	v_mbcnt_hi_u32_b32 v129, -1, v129
	s_nop 0
	v_and_b32_e32 v130, 15, v129
	v_lshrrev_b32_e32 v204, 3, v129
	v_lshl_add_u32 v205, v130, 13, s3
	v_bitop3_b32 v130, v204, v130, s42 bitop3:0x6c
	v_lshl_add_u32 v130, v130, 4, v205
	v_add_u32_e32 v206, 0, v130
	ds_read_b128 v[168:171], v206
	v_xad_u32 v172, v130, 16, 0
	ds_read_b128 v[172:175], v172
	s_waitcnt lgkmcnt(1)
	v_cvt_pk_bf16_f32 v176, v168, v169
	s_nop 0
	v_lshlrev_b32_e32 v177, 16, v176
	v_sub_f32_e32 v168, v168, v177
	v_and_b32_e32 v177, 0xffff0000, v176
	v_sub_f32_e32 v169, v169, v177
	v_cvt_pk_bf16_f32 v168, v168, v169
	v_cvt_pk_bf16_f32 v177, v170, v171
	s_nop 0
	v_lshlrev_b32_e32 v169, 16, v177
	v_sub_f32_e32 v169, v170, v169
	v_and_b32_e32 v170, 0xffff0000, v177
	v_sub_f32_e32 v170, v171, v170
	v_cvt_pk_bf16_f32 v169, v169, v170
	s_waitcnt lgkmcnt(0)
	v_cvt_pk_bf16_f32 v178, v172, v173
	s_nop 0
	v_lshlrev_b32_e32 v170, 16, v178
	v_and_b32_e32 v171, 0xffff0000, v178
	v_sub_f32_e32 v170, v172, v170
	v_sub_f32_e32 v171, v173, v171
	v_cvt_pk_bf16_f32 v170, v170, v171
	v_cvt_pk_bf16_f32 v179, v174, v175
	v_and_b32_e32 v171, 0xffffffe, v204
	v_mfma_f32_16x16x32_bf16 v[180:183], v[176:179], v[0:3], 0
	v_add_u32_e32 v171, 8, v171
	v_bitop3_b32 v129, v171, v129, 15 bitop3:0x78
	v_lshl_add_u32 v129, v129, 4, v205
	v_mfma_f32_16x16x32_bf16 v[200:203], v[176:179], v[8:11], 0
	v_lshlrev_b32_e32 v171, 16, v179
	v_sub_f32_e32 v171, v174, v171
	v_and_b32_e32 v172, 0xffff0000, v179
	v_mfma_f32_16x16x32_bf16 v[180:183], v[176:179], v[4:7], v[180:183]
	v_add_u32_e32 v204, 0, v129
	v_sub_f32_e32 v172, v175, v172
	v_cvt_pk_bf16_f32 v171, v171, v172
	v_mfma_f32_16x16x32_bf16 v[200:203], v[176:179], v[12:15], v[200:203]
	ds_read_b128 v[176:179], v204
	v_mfma_f32_16x16x32_bf16 v[172:175], v[168:171], v[0:3], v[180:183]
	s_nop 2
	v_xad_u32 v180, v129, 16, 0
	v_mfma_f32_16x16x32_bf16 v[168:171], v[168:171], v[8:11], v[200:203]
	ds_read_b128 v[180:183], v180
	s_waitcnt lgkmcnt(1)
	v_cvt_pk_bf16_f32 v200, v176, v177
	s_nop 0
	v_lshlrev_b32_e32 v201, 16, v200
	v_sub_f32_e32 v176, v176, v201
	v_and_b32_e32 v201, 0xffff0000, v200
	v_sub_f32_e32 v177, v177, v201
	v_cvt_pk_bf16_f32 v176, v176, v177
	v_cvt_pk_bf16_f32 v201, v178, v179
	s_nop 0
	v_lshlrev_b32_e32 v177, 16, v201
	v_sub_f32_e32 v177, v178, v177
	v_and_b32_e32 v178, 0xffff0000, v201
	v_sub_f32_e32 v178, v179, v178
	v_cvt_pk_bf16_f32 v177, v177, v178
	s_waitcnt lgkmcnt(0)
	v_cvt_pk_bf16_f32 v202, v180, v181
	s_nop 0
	v_lshlrev_b32_e32 v178, 16, v202
	v_sub_f32_e32 v178, v180, v178
	v_and_b32_e32 v179, 0xffff0000, v202
	v_sub_f32_e32 v179, v181, v179
	v_cvt_pk_bf16_f32 v178, v178, v179
	v_cvt_pk_bf16_f32 v203, v182, v183
	s_nop 0
	v_mfma_f32_16x16x32_bf16 v[172:175], v[200:203], v[16:19], v[172:175]
	v_lshlrev_b32_e32 v179, 16, v203
	v_and_b32_e32 v180, 0xffff0000, v203
	v_sub_f32_e32 v179, v182, v179
	v_mfma_f32_16x16x32_bf16 v[168:171], v[200:203], v[24:27], v[168:171]
	v_sub_f32_e32 v180, v183, v180
	v_cvt_pk_bf16_f32 v179, v179, v180
	ds_read_b128 v[180:183], v206 offset:256
	v_mfma_f32_16x16x32_bf16 v[172:175], v[200:203], v[20:23], v[172:175]
	v_mfma_f32_16x16x32_bf16 v[168:171], v[200:203], v[28:31], v[168:171]
	v_mfma_f32_16x16x32_bf16 v[172:175], v[176:179], v[16:19], v[172:175]
	v_mfma_f32_16x16x32_bf16 v[168:171], v[176:179], v[24:27], v[168:171]
	v_add_u32_e32 v176, 0x100, v130
	v_xad_u32 v176, v176, 16, 0
	ds_read_b128 v[176:179], v176
	s_waitcnt lgkmcnt(1)
	v_cvt_pk_bf16_f32 v200, v180, v181
	s_nop 0
	v_lshlrev_b32_e32 v201, 16, v200
	v_sub_f32_e32 v180, v180, v201
	v_and_b32_e32 v201, 0xffff0000, v200
	v_sub_f32_e32 v181, v181, v201
	v_cvt_pk_bf16_f32 v180, v180, v181
	v_cvt_pk_bf16_f32 v201, v182, v183
	s_nop 0
	v_lshlrev_b32_e32 v181, 16, v201
	v_sub_f32_e32 v181, v182, v181
	v_and_b32_e32 v182, 0xffff0000, v201
	v_sub_f32_e32 v182, v183, v182
	v_cvt_pk_bf16_f32 v181, v181, v182
	s_waitcnt lgkmcnt(0)
	v_cvt_pk_bf16_f32 v202, v176, v177
	s_nop 0
	v_lshlrev_b32_e32 v182, 16, v202
	v_sub_f32_e32 v176, v176, v182
	v_and_b32_e32 v182, 0xffff0000, v202
	v_sub_f32_e32 v177, v177, v182
	v_cvt_pk_bf16_f32 v182, v176, v177
	v_cvt_pk_bf16_f32 v203, v178, v179
	s_nop 0
	v_mfma_f32_16x16x32_bf16 v[172:175], v[200:203], v[32:35], v[172:175]
	v_lshlrev_b32_e32 v176, 16, v203
	v_and_b32_e32 v177, 0xffff0000, v203
	v_sub_f32_e32 v176, v178, v176
	v_mfma_f32_16x16x32_bf16 v[168:171], v[200:203], v[40:43], v[168:171]
	v_sub_f32_e32 v177, v179, v177
	v_cvt_pk_bf16_f32 v183, v176, v177
	ds_read_b128 v[176:179], v204 offset:256
	v_mfma_f32_16x16x32_bf16 v[172:175], v[200:203], v[36:39], v[172:175]
	v_mfma_f32_16x16x32_bf16 v[168:171], v[200:203], v[44:47], v[168:171]
	v_mfma_f32_16x16x32_bf16 v[172:175], v[180:183], v[32:35], v[172:175]
	v_mfma_f32_16x16x32_bf16 v[168:171], v[180:183], v[40:43], v[168:171]
	v_add_u32_e32 v180, 0x100, v129
	v_xad_u32 v180, v180, 16, 0
	ds_read_b128 v[180:183], v180
	s_waitcnt lgkmcnt(1)
	v_cvt_pk_bf16_f32 v200, v176, v177
	s_nop 0
	v_lshlrev_b32_e32 v201, 16, v200
	v_sub_f32_e32 v176, v176, v201
	v_and_b32_e32 v201, 0xffff0000, v200
	v_sub_f32_e32 v177, v177, v201
	v_cvt_pk_bf16_f32 v176, v176, v177
	v_cvt_pk_bf16_f32 v201, v178, v179
	s_nop 0
	v_lshlrev_b32_e32 v177, 16, v201
	v_sub_f32_e32 v177, v178, v177
	v_and_b32_e32 v178, 0xffff0000, v201
	v_sub_f32_e32 v178, v179, v178
	v_cvt_pk_bf16_f32 v177, v177, v178
	s_waitcnt lgkmcnt(0)
	v_cvt_pk_bf16_f32 v202, v180, v181
	s_nop 0
	v_lshlrev_b32_e32 v178, 16, v202
	v_sub_f32_e32 v178, v180, v178
	v_and_b32_e32 v179, 0xffff0000, v202
	v_sub_f32_e32 v179, v181, v179
	v_cvt_pk_bf16_f32 v178, v178, v179
	v_cvt_pk_bf16_f32 v203, v182, v183
	s_nop 0
	v_mfma_f32_16x16x32_bf16 v[172:175], v[200:203], v[48:51], v[172:175]
	v_lshlrev_b32_e32 v179, 16, v203
	v_and_b32_e32 v180, 0xffff0000, v203
	v_sub_f32_e32 v179, v182, v179
	v_mfma_f32_16x16x32_bf16 v[168:171], v[200:203], v[56:59], v[168:171]
	v_sub_f32_e32 v180, v183, v180
	v_cvt_pk_bf16_f32 v179, v179, v180
	ds_read_b128 v[180:183], v206 offset:512
	v_mfma_f32_16x16x32_bf16 v[172:175], v[200:203], v[52:55], v[172:175]
	v_mfma_f32_16x16x32_bf16 v[168:171], v[200:203], v[60:63], v[168:171]
	v_mfma_f32_16x16x32_bf16 v[172:175], v[176:179], v[48:51], v[172:175]
	v_mfma_f32_16x16x32_bf16 v[168:171], v[176:179], v[56:59], v[168:171]
	v_add_u32_e32 v176, 0x200, v130
	v_xad_u32 v176, v176, 16, 0
	ds_read_b128 v[176:179], v176
	s_waitcnt lgkmcnt(1)
	v_cvt_pk_bf16_f32 v200, v180, v181
	v_add_u32_e32 v130, 0x300, v130
	v_lshlrev_b32_e32 v201, 16, v200
	v_sub_f32_e32 v180, v180, v201
	v_and_b32_e32 v201, 0xffff0000, v200
	v_sub_f32_e32 v181, v181, v201
	v_cvt_pk_bf16_f32 v180, v180, v181
	v_cvt_pk_bf16_f32 v201, v182, v183
	v_xad_u32 v130, v130, 16, 0
	v_lshlrev_b32_e32 v181, 16, v201
	v_sub_f32_e32 v181, v182, v181
	v_and_b32_e32 v182, 0xffff0000, v201
	v_sub_f32_e32 v182, v183, v182
	v_cvt_pk_bf16_f32 v181, v181, v182
	s_waitcnt lgkmcnt(0)
	v_cvt_pk_bf16_f32 v202, v176, v177
	s_nop 0
	v_lshlrev_b32_e32 v182, 16, v202
	v_sub_f32_e32 v176, v176, v182
	v_and_b32_e32 v182, 0xffff0000, v202
	v_sub_f32_e32 v177, v177, v182
	v_cvt_pk_bf16_f32 v182, v176, v177
	v_cvt_pk_bf16_f32 v203, v178, v179
	s_nop 0
	v_mfma_f32_16x16x32_bf16 v[172:175], v[200:203], v[64:67], v[172:175]
	v_lshlrev_b32_e32 v176, 16, v203
	v_and_b32_e32 v177, 0xffff0000, v203
	v_sub_f32_e32 v176, v178, v176
	v_mfma_f32_16x16x32_bf16 v[168:171], v[200:203], v[72:75], v[168:171]
	v_sub_f32_e32 v177, v179, v177
	v_cvt_pk_bf16_f32 v183, v176, v177
	ds_read_b128 v[176:179], v204 offset:512
	v_mfma_f32_16x16x32_bf16 v[172:175], v[200:203], v[68:71], v[172:175]
	v_mfma_f32_16x16x32_bf16 v[168:171], v[200:203], v[76:79], v[168:171]
	v_mfma_f32_16x16x32_bf16 v[172:175], v[180:183], v[64:67], v[172:175]
	v_mfma_f32_16x16x32_bf16 v[168:171], v[180:183], v[72:75], v[168:171]
	v_add_u32_e32 v180, 0x200, v129
	v_xad_u32 v180, v180, 16, 0
	ds_read_b128 v[180:183], v180
	s_waitcnt lgkmcnt(1)
	v_cvt_pk_bf16_f32 v200, v176, v177
	v_add_u32_e32 v129, 0x300, v129
	v_lshlrev_b32_e32 v201, 16, v200
	v_sub_f32_e32 v176, v176, v201
	v_and_b32_e32 v201, 0xffff0000, v200
	v_sub_f32_e32 v177, v177, v201
	v_cvt_pk_bf16_f32 v176, v176, v177
	v_cvt_pk_bf16_f32 v201, v178, v179
	v_xad_u32 v129, v129, 16, 0
	v_lshlrev_b32_e32 v177, 16, v201
	v_sub_f32_e32 v177, v178, v177
	v_and_b32_e32 v178, 0xffff0000, v201
	v_sub_f32_e32 v178, v179, v178
	v_cvt_pk_bf16_f32 v177, v177, v178
	s_waitcnt lgkmcnt(0)
	v_cvt_pk_bf16_f32 v202, v180, v181
	s_nop 0
	v_lshlrev_b32_e32 v178, 16, v202
	v_sub_f32_e32 v178, v180, v178
	v_and_b32_e32 v179, 0xffff0000, v202
	v_sub_f32_e32 v179, v181, v179
	v_cvt_pk_bf16_f32 v178, v178, v179
	v_cvt_pk_bf16_f32 v203, v182, v183
	s_nop 0
	v_mfma_f32_16x16x32_bf16 v[172:175], v[200:203], v[80:83], v[172:175]
	v_lshlrev_b32_e32 v179, 16, v203
	v_and_b32_e32 v180, 0xffff0000, v203
	v_sub_f32_e32 v179, v182, v179
	v_mfma_f32_16x16x32_bf16 v[168:171], v[200:203], v[88:91], v[168:171]
	v_sub_f32_e32 v180, v183, v180
	v_cvt_pk_bf16_f32 v179, v179, v180
	ds_read_b128 v[180:183], v206 offset:768
	v_mfma_f32_16x16x32_bf16 v[172:175], v[200:203], v[84:87], v[172:175]
	v_mfma_f32_16x16x32_bf16 v[168:171], v[200:203], v[92:95], v[168:171]
	v_mfma_f32_16x16x32_bf16 v[172:175], v[176:179], v[80:83], v[172:175]
	v_mfma_f32_16x16x32_bf16 v[168:171], v[176:179], v[88:91], v[168:171]
	ds_read_b128 v[176:179], v130
	s_waitcnt lgkmcnt(1)
	v_cvt_pk_bf16_f32 v200, v180, v181
	s_nop 0
	v_lshlrev_b32_e32 v130, 16, v200
	v_sub_f32_e32 v130, v180, v130
	v_and_b32_e32 v180, 0xffff0000, v200
	v_sub_f32_e32 v180, v181, v180
	v_cvt_pk_bf16_f32 v180, v130, v180
	v_cvt_pk_bf16_f32 v201, v182, v183
	s_nop 0
	v_lshlrev_b32_e32 v130, 16, v201
	v_and_b32_e32 v181, 0xffff0000, v201
	v_sub_f32_e32 v130, v182, v130
	v_sub_f32_e32 v181, v183, v181
	v_cvt_pk_bf16_f32 v181, v130, v181
	s_waitcnt lgkmcnt(0)
	v_cvt_pk_bf16_f32 v202, v176, v177
	s_nop 0
	v_lshlrev_b32_e32 v130, 16, v202
	v_sub_f32_e32 v130, v176, v130
	v_and_b32_e32 v176, 0xffff0000, v202
	v_sub_f32_e32 v176, v177, v176
	v_cvt_pk_bf16_f32 v182, v130, v176
	v_cvt_pk_bf16_f32 v203, v178, v179
	s_nop 0
	v_mfma_f32_16x16x32_bf16 v[172:175], v[200:203], v[96:99], v[172:175]
	v_and_b32_e32 v176, 0xffff0000, v203
	v_lshlrev_b32_e32 v130, 16, v203
	v_sub_f32_e32 v176, v179, v176
	v_mfma_f32_16x16x32_bf16 v[168:171], v[200:203], v[104:107], v[168:171]
	v_sub_f32_e32 v130, v178, v130
	v_cvt_pk_bf16_f32 v183, v130, v176
	ds_read_b128 v[176:179], v204 offset:768
	v_mfma_f32_16x16x32_bf16 v[172:175], v[200:203], v[100:103], v[172:175]
	v_mfma_f32_16x16x32_bf16 v[168:171], v[200:203], v[108:111], v[168:171]
	v_mfma_f32_16x16x32_bf16 v[172:175], v[180:183], v[96:99], v[172:175]
	v_mfma_f32_16x16x32_bf16 v[168:171], v[180:183], v[104:107], v[168:171]
	ds_read_b128 v[180:183], v129
	s_waitcnt lgkmcnt(1)
	v_cvt_pk_bf16_f32 v200, v176, v177
	s_nop 0
	v_lshlrev_b32_e32 v129, 16, v200
	v_and_b32_e32 v130, 0xffff0000, v200
	v_sub_f32_e32 v129, v176, v129
	v_sub_f32_e32 v130, v177, v130
	v_cvt_pk_bf16_f32 v176, v129, v130
	v_cvt_pk_bf16_f32 v201, v178, v179
	s_nop 0
	v_lshlrev_b32_e32 v129, 16, v201
	v_and_b32_e32 v130, 0xffff0000, v201
	v_sub_f32_e32 v129, v178, v129
	v_sub_f32_e32 v130, v179, v130
	v_cvt_pk_bf16_f32 v177, v129, v130
	s_waitcnt lgkmcnt(0)
	v_cvt_pk_bf16_f32 v202, v180, v181
	s_nop 0
	v_lshlrev_b32_e32 v129, 16, v202
	v_and_b32_e32 v130, 0xffff0000, v202
	v_sub_f32_e32 v129, v180, v129
	v_sub_f32_e32 v130, v181, v130
	v_cvt_pk_bf16_f32 v178, v129, v130
	v_cvt_pk_bf16_f32 v203, v182, v183
	s_nop 0
	v_mfma_f32_16x16x32_bf16 v[172:175], v[200:203], v[112:115], v[172:175]
	v_lshlrev_b32_e32 v129, 16, v203
	v_and_b32_e32 v130, 0xffff0000, v203
	v_sub_f32_e32 v129, v182, v129
	v_mfma_f32_16x16x32_bf16 v[168:171], v[200:203], v[120:123], v[168:171]
	v_sub_f32_e32 v130, v183, v130
	v_cvt_pk_bf16_f32 v179, v129, v130
	v_mfma_f32_16x16x32_bf16 v[172:175], v[200:203], v[116:119], v[172:175]
	v_mfma_f32_16x16x32_bf16 v[168:171], v[200:203], v[124:127], v[168:171]
	v_mfma_f32_16x16x32_bf16 v[172:175], v[176:179], v[112:115], v[172:175]
	v_mfma_f32_16x16x32_bf16 v[168:171], v[176:179], v[120:123], v[168:171]
	s_nop 7
	ds_write2_b32 v197, v172, v168 offset1:16
	ds_write2_b32 v197, v173, v169 offset0:32 offset1:48
	ds_write2_b32 v197, v174, v170 offset0:64 offset1:80
	ds_write2_b32 v197, v175, v171 offset0:96 offset1:112
	s_waitcnt lgkmcnt(0)
	s_barrier
	v_mov_b32_e32 v129, v246
	ds_read2st64_b32 v[168:169], v191 offset1:8
	ds_read2st64_b32 v[170:171], v191 offset0:16 offset1:24
	ds_read2st64_b32 v[172:173], v191 offset0:32 offset1:40
	s_waitcnt lgkmcnt(2)
	v_add_f32_e32 v129, v129, v168
	v_add_f32_e32 v129, v129, v169
	ds_read2st64_b32 v[168:169], v191 offset0:48 offset1:56
	s_waitcnt lgkmcnt(2)
	v_add_f32_e32 v129, v129, v170
	v_add_f32_e32 v129, v129, v171
	s_waitcnt lgkmcnt(1)
	v_add_f32_e32 v129, v129, v172
	v_add_f32_e32 v129, v129, v173
	s_waitcnt lgkmcnt(0)
	v_add_f32_e32 v129, v129, v168
	v_add_f32_e32 v168, v129, v169
	v_mov_b32_e32 v170, v168
	v_mov_b32_e32 v171, v190
	s_nop 0
	v_mov_b32_dpp v170, v170 quad_perm:[1,0,3,2] row_mask:0xf bank_mask:0xf
	v_mov_b32_dpp v171, v171 quad_perm:[1,0,3,2] row_mask:0xf bank_mask:0xf
	v_cmp_lt_f32_e64 s[14:15], v168, v170
	v_cmp_nlt_f32_e32 vcc, v168, v170
	s_and_saveexec_b64 s[36:37], vcc
	v_cmp_eq_f32_e32 vcc, v168, v170
	v_cmp_lt_i32_e64 s[12:13], v171, v190
	s_and_b64 s[12:13], vcc, s[12:13]
	s_andn2_b64 s[14:15], s[14:15], exec
	s_and_b64 s[12:13], s[12:13], exec
	s_or_b64 s[14:15], s[14:15], s[12:13]
	s_or_b64 exec, exec, s[36:37]
	v_mov_b32_e32 v169, v168
	v_mov_b32_e32 v129, v190
	v_mov_b32_e32 v130, v168
	s_and_saveexec_b64 s[12:13], s[14:15]
	v_mov_b32_e32 v169, v170
	v_mov_b32_e32 v129, v171
	v_mov_b32_e32 v130, v170
	s_or_b64 exec, exec, s[12:13]
	v_mov_b32_e32 v170, v169
	v_mov_b32_e32 v171, v129
	s_nop 0
	v_mov_b32_dpp v170, v170 quad_perm:[2,3,0,1] row_mask:0xf bank_mask:0xf
	v_mov_b32_dpp v171, v171 quad_perm:[2,3,0,1] row_mask:0xf bank_mask:0xf
	v_cmp_lt_f32_e64 s[14:15], v130, v170
	v_cmp_nlt_f32_e32 vcc, v130, v170
	s_and_saveexec_b64 s[36:37], vcc
	v_cmp_eq_f32_e32 vcc, v130, v170
	v_cmp_lt_i32_e64 s[12:13], v171, v129
	s_and_b64 s[12:13], vcc, s[12:13]
	s_andn2_b64 s[14:15], s[14:15], exec
	s_and_b64 s[12:13], s[12:13], exec
	s_or_b64 s[14:15], s[14:15], s[12:13]
	s_or_b64 exec, exec, s[36:37]
	s_and_saveexec_b64 s[12:13], s[14:15]
	v_mov_b32_e32 v169, v170
	v_mov_b32_e32 v129, v171
	v_mov_b32_e32 v130, v170
	s_or_b64 exec, exec, s[12:13]
	v_mov_b32_e32 v170, v169
	v_mov_b32_e32 v171, v129
	s_nop 0
	v_mov_b32_dpp v170, v170 row_half_mirror row_mask:0xf bank_mask:0xf
	v_mov_b32_dpp v171, v171 row_half_mirror row_mask:0xf bank_mask:0xf
	v_cmp_lt_f32_e64 s[14:15], v130, v170
	v_cmp_nlt_f32_e32 vcc, v130, v170
	s_and_saveexec_b64 s[36:37], vcc
	v_cmp_eq_f32_e32 vcc, v130, v170
	v_cmp_lt_i32_e64 s[12:13], v171, v129
	s_and_b64 s[12:13], vcc, s[12:13]
	s_andn2_b64 s[14:15], s[14:15], exec
	s_and_b64 s[12:13], s[12:13], exec
	s_or_b64 s[14:15], s[14:15], s[12:13]
	s_or_b64 exec, exec, s[36:37]
	s_and_saveexec_b64 s[12:13], s[14:15]
	v_mov_b32_e32 v169, v170
	v_mov_b32_e32 v129, v171
	v_mov_b32_e32 v130, v170
	s_or_b64 exec, exec, s[12:13]
	v_mov_b32_e32 v170, v169
	v_mov_b32_e32 v171, v129
	s_nop 0
	v_mov_b32_dpp v170, v170 row_mirror row_mask:0xf bank_mask:0xf
	v_mov_b32_dpp v171, v171 row_mirror row_mask:0xf bank_mask:0xf
	v_cmp_lt_f32_e64 s[14:15], v130, v170
	v_cmp_nlt_f32_e32 vcc, v130, v170
	s_and_saveexec_b64 s[36:37], vcc
	v_cmp_eq_f32_e32 vcc, v130, v170
	v_cmp_lt_i32_e64 s[12:13], v171, v129
	s_and_b64 s[12:13], vcc, s[12:13]
	s_andn2_b64 s[14:15], s[14:15], exec
	s_and_b64 s[12:13], s[12:13], exec
	s_or_b64 s[14:15], s[14:15], s[12:13]
	s_or_b64 exec, exec, s[36:37]
	s_and_saveexec_b64 s[12:13], s[14:15]
	v_mov_b32_e32 v169, v170
	v_mov_b32_e32 v129, v171
	v_mov_b32_e32 v130, v170
	s_or_b64 exec, exec, s[12:13]
	ds_swizzle_b32 v169, v169 offset:swizzle(SWAP,16)
	ds_swizzle_b32 v170, v129 offset:swizzle(SWAP,16)
	s_waitcnt lgkmcnt(1)
	v_cmp_lt_f32_e64 s[14:15], v130, v169
	v_cmp_nlt_f32_e32 vcc, v130, v169
	s_and_saveexec_b64 s[36:37], vcc
	s_cbranch_execz .LBB0_993
	v_cmp_eq_f32_e32 vcc, v130, v169
	s_waitcnt lgkmcnt(0)
	v_cmp_lt_i32_e64 s[12:13], v170, v129
	s_and_b64 s[12:13], vcc, s[12:13]
	s_andn2_b64 s[14:15], s[14:15], exec
	s_and_b64 s[12:13], s[12:13], exec
	s_or_b64 s[14:15], s[14:15], s[12:13]
